# xnorm: x rows 2,3 of a pass requested together with rows 0,1 (into free registers) instead of after rows 0,1 were consumed; counted waits adjusted
# baseline (speedup 1.0000x reference)
; DI void phase_xnorm(const Params& p, int bid, int nb, char* lds) {
;     ...
;   for (int row0 = gw * 4; row0 < T_; row0 += nw * 4) {
;     const int b = row0 >> 13;
;     f32x4 v[4][4];
; #pragma unroll
;     for (int r = 0; r < 4; ++r)
; #pragma unroll
;       for (int i = 0; i < 4; ++i) v[r][i] = ((const f32x4*)(p.x + (size_t)(row0 + r) * 1024))[lane + 64 * i];
;     f32x4 g4[4], sh[4], sc[4];
; #pragma unroll
;     for (int i = 0; i < 4; ++i) { const int col = 4 * lane + 256 * i; g4[i] = *(const f32x4*)(p.g_pre_mix + col); sh[i] = *(const f32x4*)(mod + b * 6144 + col); sc[i] = *(const f32x4*)(mod + b * 6144 + 1024 + col); }
; #pragma unroll
;     for (int r = 0; r < 4; ++r) {
;       float ss = 0.f;
; #pragma unroll
;       for (int i = 0; i < 4; ++i) ss += v[r][i][0] * v[r][i][0] + v[r][i][1] * v[r][i][1] + v[r][i][2] * v[r][i][2] + v[r][i][3] * v[r][i][3];
;       ss = wave_sum(ss);
;       const float rstd = rsqrtf(ss * (1.f / 1024.f) + 1e-6f);
.LBB0_94:
	v_add_co_u32_e32 v0, vcc, 0xffffd000, v106
	v_ashrrev_i32_e32 v4, 13, v88
	s_nop 0
	v_addc_co_u32_e32 v1, vcc, -1, v107, vcc
	global_load_dwordx4 v[60:63], v[0:1], off offset:-3072
	global_load_dwordx4 v[56:59], v[0:1], off offset:-2048
	global_load_dwordx4 v[36:39], v[0:1], off offset:-1024
	global_load_dwordx4 v[32:35], v[0:1], off
	v_add_co_u32_e32 v0, vcc, 0xffffe000, v106
	v_mul_i32_i24_e32 v4, 0x1800, v4
	s_nop 0
	v_addc_co_u32_e32 v1, vcc, -1, v107, vcc
	global_load_dwordx4 v[52:55], v[0:1], off offset:-3072
	global_load_dwordx4 v[48:51], v[0:1], off offset:-2048
	global_load_dwordx4 v[44:47], v[0:1], off offset:-1024
	global_load_dwordx4 v[40:43], v[0:1], off
	v_ashrrev_i32_e32 v5, 31, v4
	v_lshl_add_u64 v[4:5], v[4:5], 2, s[20:21]
	v_lshl_add_u64 v[8:9], v[4:5], 0, s[24:25]
	v_mov_b32_e32 v109, v93
	v_mov_b32_e32 v111, v93
	v_mov_b32_e32 v113, v93
	v_lshl_add_u64 v[20:21], v[4:5], 0, v[92:93]
	v_lshl_add_u64 v[10:11], v[8:9], 0, v[92:93]
	global_load_dwordx4 v[0:3], v[94:95], off
	global_load_dwordx4 v[4:7], v[20:21], off
	v_lshl_add_u64 v[12:13], v[8:9], 0, v[108:109]
	v_lshl_add_u64 v[14:15], v[8:9], 0, v[110:111]
	v_lshl_add_u64 v[8:9], v[8:9], 0, v[112:113]
	global_load_dwordx4 v[72:75], v[10:11], off
	global_load_dwordx4 v[76:79], v[12:13], off
	global_load_dwordx4 v[68:71], v[14:15], off
	global_load_dwordx4 v[64:67], v[8:9], off
	v_add_co_u32_e32 v210, vcc, 0xfffff000, v106
	s_nop 1
	v_addc_co_u32_e32 v211, vcc, -1, v107, vcc
	global_load_dwordx4 v[164:167], v[210:211], off offset:-3072
	global_load_dwordx4 v[168:171], v[210:211], off offset:-2048
	global_load_dwordx4 v[172:175], v[210:211], off offset:-1024
	global_load_dwordx4 v[178:181], v[106:107], off offset:-4096
	global_load_dwordx4 v[182:185], v[106:107], off offset:-3072
	global_load_dwordx4 v[192:195], v[106:107], off offset:-2048
	global_load_dwordx4 v[196:199], v[106:107], off offset:-1024
	global_load_dwordx4 v[200:203], v[106:107], off
	v_add_co_u32_e32 v152, vcc, 0xfffff000, v106
	v_mov_b64_e32 v[126:127], s[28:29]
	s_nop 0
	v_addc_co_u32_e32 v153, vcc, -1, v107, vcc
	v_lshl_add_u64 v[134:135], s[84:85], 0, v[104:105]
	s_waitcnt vmcnt(21)
	v_mov_b32_e32 v10, v61
	s_waitcnt vmcnt(20)
	v_mov_b32_e32 v11, v57
	s_waitcnt vmcnt(19)
	v_mov_b32_e32 v18, v37
	s_waitcnt vmcnt(18)
	v_mov_b32_e32 v19, v33
	v_mov_b32_e32 v8, v60
	v_mov_b32_e32 v9, v56
	v_mov_b32_e32 v16, v36
	v_mov_b32_e32 v17, v32
	v_pk_mul_f32 v[10:11], v[10:11], v[10:11]
	v_pk_mul_f32 v[18:19], v[18:19], v[18:19]
	s_waitcnt vmcnt(17)
	v_mov_b32_e32 v28, v53
	s_waitcnt vmcnt(16)
	v_mov_b32_e32 v29, v49
	v_mov_b32_e32 v12, v62
	v_mov_b32_e32 v13, v58
	v_mov_b32_e32 v26, v52
	v_mov_b32_e32 v27, v48
	s_waitcnt vmcnt(15)
	v_mov_b32_e32 v84, v45
	s_waitcnt vmcnt(14)
	v_mov_b32_e32 v85, v41
	v_pk_fma_f32 v[8:9], v[8:9], v[8:9], v[10:11]
	v_pk_fma_f32 v[10:11], v[16:17], v[16:17], v[18:19]
	v_pk_mul_f32 v[16:17], v[28:29], v[28:29]
	v_mov_b32_e32 v30, v54
	v_mov_b32_e32 v31, v50
	v_mov_b32_e32 v82, v44
	v_mov_b32_e32 v83, v40
	v_pk_mul_f32 v[18:19], v[84:85], v[84:85]
	v_pk_fma_f32 v[8:9], v[12:13], v[12:13], v[8:9]
	v_pk_fma_f32 v[12:13], v[26:27], v[26:27], v[16:17]
	v_mov_b32_e32 v14, v63
	v_mov_b32_e32 v15, v59
	v_mov_b32_e32 v22, v38
	v_mov_b32_e32 v23, v34
	v_mov_b32_e32 v80, v55
	v_mov_b32_e32 v81, v51
	v_mov_b32_e32 v86, v46
	v_mov_b32_e32 v87, v42
	v_pk_fma_f32 v[16:17], v[82:83], v[82:83], v[18:19]
	v_pk_fma_f32 v[12:13], v[30:31], v[30:31], v[12:13]
	v_mov_b32_e32 v24, v39
	v_mov_b32_e32 v25, v35
	v_mov_b32_e32 v116, v47
	v_mov_b32_e32 v117, v43
	v_pk_fma_f32 v[10:11], v[22:23], v[22:23], v[10:11]
	v_pk_fma_f32 v[8:9], v[14:15], v[14:15], v[8:9]
	v_pk_fma_f32 v[14:15], v[86:87], v[86:87], v[16:17]
	v_pk_fma_f32 v[12:13], v[80:81], v[80:81], v[12:13]
	v_pk_fma_f32 v[10:11], v[24:25], v[24:25], v[10:11]
	v_pk_fma_f32 v[14:15], v[116:117], v[116:117], v[14:15]
	v_mov_b32_e32 v17, v8
	v_mov_b32_e32 v16, v12
	v_mov_b32_e32 v8, v13
	v_mov_b32_e32 v12, v14
	v_pk_add_f32 v[8:9], v[16:17], v[8:9]
	v_mov_b32_e32 v13, v10
	v_pk_add_f32 v[8:9], v[8:9], v[12:13]
	v_mov_b32_e32 v10, v15
	v_pk_add_f32 v[8:9], v[8:9], v[10:11]
	ds_bpermute_b32 v11, v91, v9
	ds_bpermute_b32 v10, v91, v8
	s_waitcnt vmcnt(11)
	v_pk_add_f32 v[122:123], v[74:75], 1.0 op_sel_hi:[1,0]
	s_waitcnt vmcnt(9)
	v_pk_add_f32 v[116:117], v[70:71], 1.0 op_sel_hi:[1,0]
	v_pk_add_f32 v[124:125], v[72:73], 1.0 op_sel_hi:[1,0]
	v_pk_add_f32 v[118:119], v[78:79], 1.0 op_sel_hi:[1,0]
	s_waitcnt lgkmcnt(0)
	v_pk_add_f32 v[8:9], v[8:9], v[10:11]
	ds_bpermute_b32 v11, v136, v9
	ds_bpermute_b32 v10, v136, v8
	v_pk_add_f32 v[120:121], v[76:77], 1.0 op_sel_hi:[1,0]
	s_waitcnt vmcnt(0)
	v_pk_add_f32 v[130:131], v[64:65], 1.0 op_sel_hi:[1,0]
	v_pk_add_f32 v[132:133], v[68:69], 1.0 op_sel_hi:[1,0]
	v_pk_add_f32 v[128:129], v[66:67], 1.0 op_sel_hi:[1,0]
	s_waitcnt lgkmcnt(0)
	v_pk_add_f32 v[22:23], v[8:9], v[10:11]
	ds_bpermute_b32 v25, v137, v23
	ds_bpermute_b32 v24, v137, v22
	global_load_dwordx4 v[16:19], v[94:95], off offset:1024
	global_load_dwordx4 v[12:15], v[94:95], off offset:2048
	global_load_dwordx4 v[8:11], v[94:95], off offset:3072
	global_load_dwordx4 v[28:31], v[20:21], off offset:1024
	s_waitcnt lgkmcnt(0)
	v_pk_add_f32 v[22:23], v[22:23], v[24:25]
	ds_bpermute_b32 v81, v138, v23
	ds_bpermute_b32 v80, v138, v22
	global_load_dwordx4 v[24:27], v[20:21], off offset:2048
	s_waitcnt lgkmcnt(0)
	v_pk_add_f32 v[80:81], v[22:23], v[80:81]
	ds_bpermute_b32 v83, v139, v81
	ds_bpermute_b32 v82, v139, v80
	global_load_dwordx4 v[20:23], v[20:21], off offset:3072
	s_waitcnt lgkmcnt(0)
; DI unsigned pk2(float lo, float hi) { f32x2 v = {lo, hi}; bf16x2_t b = __builtin_convertvector(v, bf16x2_t); return __builtin_bit_cast(unsigned, b); }
; DI void phase_xnorm(const Params& p, int bid, int nb, char* lds) {
;     ...
;     for (int r = 0; r < 4; ++r)
; #pragma unroll
;       for (int i = 0; i < 4; ++i) v[r][i] = ((const f32x4*)(p.x + (size_t)(row0 + r) * 1024))[lane + 64 * i];
;     f32x4 g4[4], sh[4], sc[4];
; #pragma unroll
;     for (int i = 0; i < 4; ++i) { const int col = 4 * lane + 256 * i; g4[i] = *(const f32x4*)(p.g_pre_mix + col); sh[i] = *(const f32x4*)(mod + b * 6144 + col); sc[i] = *(const f32x4*)(mod + b * 6144 + 1024 + col); }
; #pragma unroll
;     for (int r = 0; r < 4; ++r) {
;       float ss = 0.f;
; #pragma unroll
;       for (int i = 0; i < 4; ++i) ss += v[r][i][0] * v[r][i][0] + v[r][i][1] * v[r][i][1] + v[r][i][2] * v[r][i][2] + v[r][i][3] * v[r][i][3];
;       ss = wave_sum(ss);
;       const float rstd = rsqrtf(ss * (1.f / 1024.f) + 1e-6f);
; #pragma unroll
;       for (int i = 0; i < 4; ++i) {
;         const f32x4 y = (v[r][i] * rstd * g4[i]) * (1.f + sc[i]) + sh[i];
;         u32x2 o = {pk2(y[0], y[1]), pk2(y[2], y[3])};
;         *(u32x2*)(h + (size_t)(row0 + r) * 1024 + 4 * lane + 256 * i) = o;
;         *(u32x2*)(yt + r * WP + 2 * (4 * lane + 256 * i)) = o;
;       }
	v_pk_add_f32 v[74:75], v[80:81], v[82:83]
	ds_bpermute_b32 v81, v140, v75
	ds_bpermute_b32 v80, v140, v74
	s_waitcnt lgkmcnt(0)
	v_pk_add_f32 v[70:71], v[74:75], v[80:81]
	s_nop 0
	v_pk_fma_f32 v[154:155], v[70:71], s[26:27], v[126:127] op_sel_hi:[1,0,0]
	v_mov_b32_e32 v84, v164
	v_mov_b32_e32 v85, v165
	v_mov_b32_e32 v86, v166
	v_mov_b32_e32 v87, v167
	v_mov_b32_e32 v80, v168
	v_mov_b32_e32 v81, v169
	v_mov_b32_e32 v82, v170
	v_mov_b32_e32 v83, v171
	v_mul_f32_e32 v70, 0x4b800000, v155
	v_cmp_gt_f32_e32 vcc, s2, v155
	v_mov_b32_e32 v76, v172
	v_mov_b32_e32 v77, v173
	v_mov_b32_e32 v78, v174
	v_mov_b32_e32 v79, v175
	v_mov_b32_e32 v72, v178
	v_mov_b32_e32 v73, v179
	v_mov_b32_e32 v74, v180
	v_mov_b32_e32 v75, v181
	v_cndmask_b32_e32 v70, v155, v70, vcc
	v_rsq_f32_e32 v70, v70
	v_mul_f32_e32 v109, 0x4b800000, v154
	v_mul_f32_e32 v64, 0x45800000, v70
	v_cndmask_b32_e32 v156, v70, v64, vcc
	v_pk_mul_f32 v[62:63], v[62:63], v[156:157] op_sel_hi:[1,0]
	v_pk_mul_f32 v[60:61], v[60:61], v[156:157] op_sel_hi:[1,0]
	v_mov_b32_e32 v68, v182
	v_mov_b32_e32 v69, v183
	v_mov_b32_e32 v70, v184
	v_mov_b32_e32 v71, v185
	v_mov_b32_e32 v64, v192
	v_mov_b32_e32 v65, v193
	v_mov_b32_e32 v66, v194
	v_mov_b32_e32 v67, v195
	v_pk_mul_f32 v[60:61], v[0:1], v[60:61]
	v_pk_mul_f32 v[62:63], v[2:3], v[62:63]
	v_pk_fma_f32 v[60:61], v[124:125], v[60:61], v[4:5]
	v_pk_fma_f32 v[62:63], v[122:123], v[62:63], v[6:7]
	v_cvt_pk_bf16_f32 v152, v60, v61
	v_cvt_pk_bf16_f32 v153, v62, v63
	v_pk_mul_f32 v[160:161], v[58:59], v[156:157] op_sel_hi:[1,0]
	v_pk_mul_f32 v[162:163], v[56:57], v[156:157] op_sel_hi:[1,0]
	v_mov_b32_e32 v60, v196
	v_mov_b32_e32 v61, v197
	v_mov_b32_e32 v62, v198
	v_mov_b32_e32 v63, v199
	v_mov_b32_e32 v56, v200
	v_mov_b32_e32 v57, v201
	v_mov_b32_e32 v58, v202
	v_mov_b32_e32 v59, v203
	v_add_co_u32_e32 v158, vcc, s3, v134
	v_pk_mul_f32 v[34:35], v[34:35], v[156:157] op_sel_hi:[1,0]
	s_nop 0
	v_addc_co_u32_e32 v159, vcc, 0, v135, vcc
	v_add_co_u32_e32 v134, vcc, s11, v134
	v_pk_mul_f32 v[32:33], v[32:33], v[156:157] op_sel_hi:[1,0]
	s_nop 0
	v_addc_co_u32_e32 v135, vcc, 0, v135, vcc
	v_cmp_gt_f32_e32 vcc, s2, v154
	v_pk_mul_f32 v[38:39], v[38:39], v[156:157] op_sel_hi:[1,0]
	v_pk_mul_f32 v[36:37], v[36:37], v[156:157] op_sel_hi:[1,0]
	v_cndmask_b32_e32 v109, v154, v109, vcc
	v_rsq_f32_e32 v109, v109
	global_store_dwordx2 v[134:135], v[152:153], off offset:-4096
	v_mul_f32_e32 v111, 0x45800000, v109
	v_cndmask_b32_e32 v154, v109, v111, vcc
	v_add_u32_e32 v109, v90, v141
	v_pk_mul_f32 v[54:55], v[54:55], v[154:155] op_sel_hi:[1,0]
	v_pk_mul_f32 v[52:53], v[52:53], v[154:155] op_sel_hi:[1,0]
	v_pk_mul_f32 v[50:51], v[50:51], v[154:155] op_sel_hi:[1,0]
	v_pk_mul_f32 v[48:49], v[48:49], v[154:155] op_sel_hi:[1,0]
	v_pk_mul_f32 v[46:47], v[46:47], v[154:155] op_sel_hi:[1,0]
	v_pk_mul_f32 v[44:45], v[44:45], v[154:155] op_sel_hi:[1,0]
	v_pk_mul_f32 v[42:43], v[42:43], v[154:155] op_sel_hi:[1,0]
	v_pk_mul_f32 v[40:41], v[40:41], v[154:155] op_sel_hi:[1,0]
	s_waitcnt vmcnt(1)
	v_pk_mul_f32 v[36:37], v[12:13], v[36:37]
	s_waitcnt vmcnt(12)
	v_pk_mul_f32 v[32:33], v[8:9], v[32:33]
	v_pk_mul_f32 v[34:35], v[10:11], v[34:35]
	v_pk_mul_f32 v[38:39], v[14:15], v[38:39]
	ds_write_b64 v109, v[152:153] offset:33024
	v_pk_mul_f32 v[152:153], v[16:17], v[162:163]
	v_pk_mul_f32 v[154:155], v[18:19], v[160:161]
	s_waitcnt vmcnt(11)
	v_pk_fma_f32 v[152:153], v[120:121], v[152:153], v[28:29]
	s_waitcnt vmcnt(10)
	v_pk_fma_f32 v[38:39], v[116:117], v[38:39], v[26:27]
	v_pk_fma_f32 v[36:37], v[132:133], v[36:37], v[24:25]
	v_pk_fma_f32 v[154:155], v[118:119], v[154:155], v[30:31]
	v_cvt_pk_bf16_f32 v36, v36, v37
	v_cvt_pk_bf16_f32 v37, v38, v39
	global_store_dwordx2 v[158:159], v[36:37], off offset:1024
	ds_write_b64 v142, v[36:37] offset:33024
	s_waitcnt vmcnt(10)
	v_pk_fma_f32 v[34:35], v[128:129], v[34:35], v[22:23]
	v_pk_fma_f32 v[32:33], v[130:131], v[32:33], v[20:21]
	v_cvt_pk_bf16_f32 v152, v152, v153
	v_cvt_pk_bf16_f32 v32, v32, v33
	v_cvt_pk_bf16_f32 v33, v34, v35
	global_store_dwordx2 v[158:159], v[32:33], off offset:1536
	ds_write_b64 v143, v[32:33] offset:33024
	v_cvt_pk_bf16_f32 v153, v154, v155
	global_store_dwordx2 v[158:159], v[152:153], off offset:512
	ds_write_b64 v89, v[152:153] offset:33024
	s_waitcnt vmcnt(11)
	v_mov_b32_e32 v34, v85
	s_waitcnt vmcnt(10)
	v_mov_b32_e32 v35, v81
	v_mov_b32_e32 v32, v84
	v_mov_b32_e32 v33, v80
	v_pk_mul_f32 v[34:35], v[34:35], v[34:35]
	s_waitcnt vmcnt(9)
	v_mov_b32_e32 v36, v77
	v_pk_fma_f32 v[32:33], v[32:33], v[32:33], v[34:35]
	v_mov_b32_e32 v34, v86
	v_mov_b32_e32 v35, v82
	v_pk_fma_f32 v[32:33], v[34:35], v[34:35], v[32:33]
	v_mov_b32_e32 v34, v87
	v_mov_b32_e32 v35, v83
	s_waitcnt vmcnt(8)
	v_mov_b32_e32 v37, v73
	v_pk_fma_f32 v[32:33], v[34:35], v[34:35], v[32:33]
	v_mov_b32_e32 v34, v76
	v_mov_b32_e32 v35, v72
	v_pk_mul_f32 v[36:37], v[36:37], v[36:37]
	s_waitcnt vmcnt(7)
	v_mov_b32_e32 v38, v69
	v_pk_fma_f32 v[34:35], v[34:35], v[34:35], v[36:37]
	v_mov_b32_e32 v36, v78
	v_mov_b32_e32 v37, v74
	v_pk_fma_f32 v[34:35], v[36:37], v[36:37], v[34:35]
	v_mov_b32_e32 v36, v79
	v_mov_b32_e32 v37, v75
	s_waitcnt vmcnt(6)
	v_mov_b32_e32 v39, v65
	v_pk_fma_f32 v[34:35], v[36:37], v[36:37], v[34:35]
	v_mov_b32_e32 v36, v68
	v_mov_b32_e32 v37, v64
	v_pk_mul_f32 v[38:39], v[38:39], v[38:39]
	s_waitcnt vmcnt(5)
	v_mov_b32_e32 v152, v61
	v_pk_fma_f32 v[36:37], v[36:37], v[36:37], v[38:39]
	v_mov_b32_e32 v38, v70
	v_mov_b32_e32 v39, v66
	v_pk_fma_f32 v[36:37], v[38:39], v[38:39], v[36:37]
	v_mov_b32_e32 v38, v71
	v_mov_b32_e32 v39, v67
	s_waitcnt vmcnt(4)
; DI unsigned pk2(float lo, float hi) { f32x2 v = {lo, hi}; bf16x2_t b = __builtin_convertvector(v, bf16x2_t); return __builtin_bit_cast(unsigned, b); }
; DI void phase_xnorm(const Params& p, int bid, int nb, char* lds) {
;     ...
;     for (int r = 0; r < 4; ++r) {
;       float ss = 0.f;
; #pragma unroll
;       for (int i = 0; i < 4; ++i) ss += v[r][i][0] * v[r][i][0] + v[r][i][1] * v[r][i][1] + v[r][i][2] * v[r][i][2] + v[r][i][3] * v[r][i][3];
;       ss = wave_sum(ss);
;       const float rstd = rsqrtf(ss * (1.f / 1024.f) + 1e-6f);
; #pragma unroll
;       for (int i = 0; i < 4; ++i) {
;         const f32x4 y = (v[r][i] * rstd * g4[i]) * (1.f + sc[i]) + sh[i];
;         u32x2 o = {pk2(y[0], y[1]), pk2(y[2], y[3])};
;         *(u32x2*)(h + (size_t)(row0 + r) * 1024 + 4 * lane + 256 * i) = o;
;         *(u32x2*)(yt + r * WP + 2 * (4 * lane + 256 * i)) = o;
;       }
	v_mov_b32_e32 v153, v57
	v_pk_fma_f32 v[36:37], v[38:39], v[38:39], v[36:37]
	v_mov_b32_e32 v38, v60
	v_mov_b32_e32 v39, v56
	v_pk_mul_f32 v[152:153], v[152:153], v[152:153]
	s_nop 0
	v_pk_fma_f32 v[38:39], v[38:39], v[38:39], v[152:153]
	v_mov_b32_e32 v152, v62
	v_mov_b32_e32 v153, v58
	v_pk_fma_f32 v[38:39], v[152:153], v[152:153], v[38:39]
	v_mov_b32_e32 v152, v63
	v_mov_b32_e32 v153, v59
	v_pk_fma_f32 v[38:39], v[152:153], v[152:153], v[38:39]
	v_mov_b32_e32 v152, v36
	v_mov_b32_e32 v153, v32
	v_mov_b32_e32 v32, v37
	v_pk_add_f32 v[32:33], v[152:153], v[32:33]
	v_mov_b32_e32 v36, v38
	v_mov_b32_e32 v37, v34
	v_pk_add_f32 v[32:33], v[32:33], v[36:37]
	v_mov_b32_e32 v34, v39
	v_pk_add_f32 v[32:33], v[32:33], v[34:35]
	ds_bpermute_b32 v35, v91, v33
	ds_bpermute_b32 v34, v91, v32
	v_pk_mul_f32 v[36:37], v[0:1], v[52:53]
	v_pk_mul_f32 v[38:39], v[2:3], v[54:55]
	v_pk_fma_f32 v[36:37], v[124:125], v[36:37], v[4:5]
	v_pk_fma_f32 v[38:39], v[122:123], v[38:39], v[6:7]
	s_waitcnt lgkmcnt(0)
	v_pk_add_f32 v[32:33], v[32:33], v[34:35]
	ds_bpermute_b32 v35, v136, v33
	ds_bpermute_b32 v34, v136, v32
	v_cvt_pk_bf16_f32 v36, v36, v37
	v_cvt_pk_bf16_f32 v37, v38, v39
	global_store_dwordx2 v[158:159], v[36:37], off offset:2048
	ds_write_b64 v109, v[36:37] offset:35088
	s_waitcnt lgkmcnt(1)
	v_pk_add_f32 v[32:33], v[32:33], v[34:35]
	ds_bpermute_b32 v35, v137, v33
	ds_bpermute_b32 v34, v137, v32
	v_pk_mul_f32 v[36:37], v[16:17], v[48:49]
	v_pk_mul_f32 v[38:39], v[18:19], v[50:51]
	v_pk_fma_f32 v[36:37], v[120:121], v[36:37], v[28:29]
	v_pk_fma_f32 v[38:39], v[118:119], v[38:39], v[30:31]
	s_waitcnt lgkmcnt(0)
	v_pk_add_f32 v[32:33], v[32:33], v[34:35]
	ds_bpermute_b32 v35, v138, v33
	ds_bpermute_b32 v34, v138, v32
	v_cvt_pk_bf16_f32 v36, v36, v37
	v_cvt_pk_bf16_f32 v37, v38, v39
	global_store_dwordx2 v[158:159], v[36:37], off offset:2560
	ds_write_b64 v89, v[36:37] offset:35088
	s_waitcnt lgkmcnt(1)
	v_pk_add_f32 v[32:33], v[32:33], v[34:35]
	ds_bpermute_b32 v35, v139, v33
	ds_bpermute_b32 v34, v139, v32
	v_pk_mul_f32 v[36:37], v[12:13], v[44:45]
	v_pk_mul_f32 v[38:39], v[14:15], v[46:47]
	v_pk_fma_f32 v[36:37], v[132:133], v[36:37], v[24:25]
	v_pk_fma_f32 v[38:39], v[116:117], v[38:39], v[26:27]
	s_waitcnt lgkmcnt(0)
	v_pk_add_f32 v[32:33], v[32:33], v[34:35]
	ds_bpermute_b32 v35, v140, v33
	ds_bpermute_b32 v34, v140, v32
	v_cvt_pk_bf16_f32 v36, v36, v37
	v_cvt_pk_bf16_f32 v37, v38, v39
	global_store_dwordx2 v[158:159], v[36:37], off offset:3072
	ds_write_b64 v142, v[36:37] offset:35088
	s_waitcnt lgkmcnt(1)
	v_pk_add_f32 v[32:33], v[32:33], v[34:35]
	v_pk_mul_f32 v[34:35], v[8:9], v[40:41]
	v_pk_fma_f32 v[32:33], v[32:33], s[26:27], v[126:127] op_sel_hi:[1,0,0]
	v_pk_fma_f32 v[34:35], v[130:131], v[34:35], v[20:21]
	v_cmp_gt_f32_e32 vcc, s2, v33
	v_cvt_pk_bf16_f32 v34, v34, v35
	v_mul_f32_e32 v35, 0x4b800000, v33
	v_cndmask_b32_e32 v33, v33, v35, vcc
	v_rsq_f32_e32 v33, v33
	v_pk_mul_f32 v[36:37], v[10:11], v[42:43]
	s_nop 0
	v_pk_fma_f32 v[36:37], v[128:129], v[36:37], v[22:23]
	s_nop 0
	v_cvt_pk_bf16_f32 v35, v36, v37
	global_store_dwordx2 v[158:159], v[34:35], off offset:3584
	ds_write_b64 v143, v[34:35] offset:35088
	v_mul_f32_e32 v34, 0x45800000, v33
	v_cndmask_b32_e32 v34, v33, v34, vcc
	v_pk_mul_f32 v[36:37], v[86:87], v[34:35] op_sel_hi:[1,0]
	v_pk_mul_f32 v[38:39], v[84:85], v[34:35] op_sel_hi:[1,0]
	v_pk_mul_f32 v[36:37], v[2:3], v[36:37]
	v_pk_mul_f32 v[38:39], v[0:1], v[38:39]
	v_pk_fma_f32 v[36:37], v[122:123], v[36:37], v[6:7]
	v_pk_fma_f32 v[38:39], v[124:125], v[38:39], v[4:5]
	v_mul_f32_e32 v33, 0x4b800000, v32
	v_cvt_pk_bf16_f32 v38, v38, v39
	v_cvt_pk_bf16_f32 v39, v36, v37
	global_store_dwordx2 v[134:135], v[38:39], off
	ds_write_b64 v109, v[38:39] offset:37152
	v_pk_mul_f32 v[36:37], v[82:83], v[34:35] op_sel_hi:[1,0]
	v_pk_mul_f32 v[38:39], v[80:81], v[34:35] op_sel_hi:[1,0]
	v_pk_mul_f32 v[36:37], v[18:19], v[36:37]
	v_pk_mul_f32 v[38:39], v[16:17], v[38:39]
	v_pk_fma_f32 v[36:37], v[118:119], v[36:37], v[30:31]
	v_pk_fma_f32 v[38:39], v[120:121], v[38:39], v[28:29]
	v_cmp_gt_f32_e32 vcc, s2, v32
	v_cvt_pk_bf16_f32 v38, v38, v39
	v_cvt_pk_bf16_f32 v39, v36, v37
	global_store_dwordx2 v[134:135], v[38:39], off offset:512
	ds_write_b64 v89, v[38:39] offset:37152
	v_pk_mul_f32 v[36:37], v[78:79], v[34:35] op_sel_hi:[1,0]
	v_pk_mul_f32 v[38:39], v[76:77], v[34:35] op_sel_hi:[1,0]
	v_cndmask_b32_e32 v32, v32, v33, vcc
	v_pk_mul_f32 v[38:39], v[12:13], v[38:39]
	v_pk_mul_f32 v[36:37], v[14:15], v[36:37]
	v_rsq_f32_e32 v32, v32
	v_pk_fma_f32 v[36:37], v[116:117], v[36:37], v[26:27]
	v_pk_fma_f32 v[38:39], v[132:133], v[38:39], v[24:25]
	v_mul_f32_e32 v33, 0x45800000, v32
	v_cvt_pk_bf16_f32 v38, v38, v39
	v_cvt_pk_bf16_f32 v39, v36, v37
	v_pk_mul_f32 v[36:37], v[74:75], v[34:35] op_sel_hi:[1,0]
	v_pk_mul_f32 v[34:35], v[72:73], v[34:35] op_sel_hi:[1,0]
	v_pk_mul_f32 v[36:37], v[10:11], v[36:37]
	v_pk_mul_f32 v[34:35], v[8:9], v[34:35]
	v_pk_fma_f32 v[36:37], v[128:129], v[36:37], v[22:23]
	v_pk_fma_f32 v[34:35], v[130:131], v[34:35], v[20:21]
	v_cndmask_b32_e32 v32, v32, v33, vcc
	v_cvt_pk_bf16_f32 v34, v34, v35
	v_cvt_pk_bf16_f32 v35, v36, v37
	global_store_dwordx2 v[134:135], v[34:35], off offset:1536
	ds_write_b64 v143, v[34:35] offset:37152
	v_pk_mul_f32 v[34:35], v[70:71], v[32:33] op_sel_hi:[1,0]
	v_pk_mul_f32 v[36:37], v[68:69], v[32:33] op_sel_hi:[1,0]
	v_pk_mul_f32 v[2:3], v[2:3], v[34:35]
	v_pk_mul_f32 v[0:1], v[0:1], v[36:37]
	v_pk_fma_f32 v[2:3], v[122:123], v[2:3], v[6:7]
	v_pk_fma_f32 v[0:1], v[124:125], v[0:1], v[4:5]
	global_store_dwordx2 v[134:135], v[38:39], off offset:1024
	v_cvt_pk_bf16_f32 v0, v0, v1
; DI unsigned pk2(float lo, float hi) { f32x2 v = {lo, hi}; bf16x2_t b = __builtin_convertvector(v, bf16x2_t); return __builtin_bit_cast(unsigned, b); }
; #define MFMA16(a, b, c) __builtin_amdgcn_mfma_f32_16x16x32_bf16((a), (b), (c), 0, 0, 0)
; DI void phase_xnorm(const Params& p, int bid, int nb, char* lds) {
;     ...
; #pragma unroll
;       for (int i = 0; i < 4; ++i) {
;         const f32x4 y = (v[r][i] * rstd * g4[i]) * (1.f + sc[i]) + sh[i];
;         u32x2 o = {pk2(y[0], y[1]), pk2(y[2], y[3])};
;         *(u32x2*)(h + (size_t)(row0 + r) * 1024 + 4 * lane + 256 * i) = o;
;         *(u32x2*)(yt + r * WP + 2 * (4 * lane + 256 * i)) = o;
;       }
;     }
;     asm volatile("" ::: "memory");
;     f32x4 acc = {0.f, 0.f, 0.f, 0.f};
;     const char* ya = yt + (fr & 3) * WP + fq * 16; const char* wb = w16 + fr * WP + fq * 16;
; #pragma unroll
;     for (int kb = 0; kb < 4; ++kb) {
;       bf16x8 fa[8], fb[8];
; #pragma unroll
;       for (int q = 0; q < 8; ++q) { fa[q] = *(const bf16x8*)(ya + (8 * kb + q) * 64); fb[q] = *(const bf16x8*)(wb + (8 * kb + q) * 64); }
; #pragma unroll
;       for (int q = 0; q < 8; ++q) acc = MFMA16(fa[q], fb[q], acc);
	v_cvt_pk_bf16_f32 v1, v2, v3
	global_store_dwordx2 v[134:135], v[0:1], off offset:2048
	ds_write_b64 v109, v[0:1] offset:39216
	v_pk_mul_f32 v[0:1], v[66:67], v[32:33] op_sel_hi:[1,0]
	v_pk_mul_f32 v[2:3], v[64:65], v[32:33] op_sel_hi:[1,0]
	v_pk_mul_f32 v[0:1], v[18:19], v[0:1]
	v_pk_mul_f32 v[2:3], v[16:17], v[2:3]
	v_pk_fma_f32 v[0:1], v[118:119], v[0:1], v[30:31]
	v_pk_fma_f32 v[2:3], v[120:121], v[2:3], v[28:29]
	ds_write_b64 v142, v[38:39] offset:37152
	v_cvt_pk_bf16_f32 v2, v2, v3
	v_cvt_pk_bf16_f32 v3, v0, v1
	global_store_dwordx2 v[134:135], v[2:3], off offset:2560
	ds_write_b64 v89, v[2:3] offset:39216
	v_pk_mul_f32 v[0:1], v[62:63], v[32:33] op_sel_hi:[1,0]
	v_pk_mul_f32 v[2:3], v[60:61], v[32:33] op_sel_hi:[1,0]
	v_pk_mul_f32 v[0:1], v[14:15], v[0:1]
	v_pk_mul_f32 v[2:3], v[12:13], v[2:3]
	v_pk_fma_f32 v[0:1], v[116:117], v[0:1], v[26:27]
	v_pk_fma_f32 v[2:3], v[132:133], v[2:3], v[24:25]
	s_nop 0
	v_cvt_pk_bf16_f32 v2, v2, v3
	v_cvt_pk_bf16_f32 v3, v0, v1
	global_store_dwordx2 v[134:135], v[2:3], off offset:3072
	ds_write_b64 v142, v[2:3] offset:39216
	v_pk_mul_f32 v[0:1], v[58:59], v[32:33] op_sel_hi:[1,0]
	v_pk_mul_f32 v[2:3], v[56:57], v[32:33] op_sel_hi:[1,0]
	v_pk_mul_f32 v[0:1], v[10:11], v[0:1]
	v_pk_mul_f32 v[2:3], v[8:9], v[2:3]
	v_pk_fma_f32 v[0:1], v[128:129], v[0:1], v[22:23]
	v_pk_fma_f32 v[2:3], v[130:131], v[2:3], v[20:21]
	s_nop 0
	v_cvt_pk_bf16_f32 v2, v2, v3
	v_cvt_pk_bf16_f32 v3, v0, v1
	global_store_dwordx2 v[134:135], v[2:3], off offset:3584
	ds_write_b64 v143, v[2:3] offset:39216
	ds_read_b128 v[0:3], v144 offset:33024
	ds_read_b128 v[4:7], v144 offset:33088
	ds_read_b128 v[8:11], v145
	ds_read_b128 v[12:15], v145 offset:64
	s_waitcnt lgkmcnt(1)
	v_mfma_f32_16x16x32_bf16 v[0:3], v[0:3], v[8:11], 0
	ds_read_b128 v[8:11], v144 offset:33152
	ds_read_b128 v[16:19], v144 offset:33216
	s_waitcnt lgkmcnt(2)
	v_mfma_f32_16x16x32_bf16 v[0:3], v[4:7], v[12:15], v[0:3]
	ds_read_b128 v[4:7], v145 offset:128
	ds_read_b128 v[12:15], v145 offset:192
	s_waitcnt lgkmcnt(1)
	v_mfma_f32_16x16x32_bf16 v[0:3], v[8:11], v[4:7], v[0:3]
	ds_read_b128 v[4:7], v144 offset:33280
	ds_read_b128 v[8:11], v144 offset:33344
	s_waitcnt lgkmcnt(2)
	v_mfma_f32_16x16x32_bf16 v[0:3], v[16:19], v[12:15], v[0:3]
	ds_read_b128 v[12:15], v145 offset:256
	ds_read_b128 v[16:19], v145 offset:320
	s_waitcnt lgkmcnt(1)
	v_mfma_f32_16x16x32_bf16 v[0:3], v[4:7], v[12:15], v[0:3]
	ds_read_b128 v[4:7], v144 offset:33408
	ds_read_b128 v[12:15], v144 offset:33472
	s_waitcnt lgkmcnt(2)
	v_mfma_f32_16x16x32_bf16 v[0:3], v[8:11], v[16:19], v[0:3]
	ds_read_b128 v[8:11], v145 offset:384
	ds_read_b128 v[16:19], v145 offset:448
	s_waitcnt lgkmcnt(1)
	v_mfma_f32_16x16x32_bf16 v[0:3], v[4:7], v[8:11], v[0:3]
	ds_read_b128 v[4:7], v144 offset:33536
	s_waitcnt lgkmcnt(1)
	v_mfma_f32_16x16x32_bf16 v[0:3], v[12:15], v[16:19], v[0:3]
	ds_read_b128 v[8:11], v144 offset:33600
	ds_read_b128 v[12:15], v145 offset:512
	ds_read_b128 v[16:19], v145 offset:576
	s_waitcnt lgkmcnt(1)
	v_mfma_f32_16x16x32_bf16 v[0:3], v[4:7], v[12:15], v[0:3]
	ds_read_b128 v[4:7], v144 offset:33664
	ds_read_b128 v[12:15], v144 offset:33728
	s_waitcnt lgkmcnt(2)
	v_mfma_f32_16x16x32_bf16 v[0:3], v[8:11], v[16:19], v[0:3]
	ds_read_b128 v[8:11], v145 offset:640
	ds_read_b128 v[16:19], v145 offset:704
	s_waitcnt lgkmcnt(1)
	v_mfma_f32_16x16x32_bf16 v[0:3], v[4:7], v[8:11], v[0:3]
	ds_read_b128 v[4:7], v144 offset:33792
	ds_read_b128 v[8:11], v144 offset:33856
	s_waitcnt lgkmcnt(2)
	v_mfma_f32_16x16x32_bf16 v[0:3], v[12:15], v[16:19], v[0:3]
	ds_read_b128 v[12:15], v145 offset:768
	ds_read_b128 v[16:19], v145 offset:832
	s_waitcnt lgkmcnt(1)
	v_mfma_f32_16x16x32_bf16 v[0:3], v[4:7], v[12:15], v[0:3]
	ds_read_b128 v[4:7], v144 offset:33920
	ds_read_b128 v[12:15], v144 offset:33984
	s_waitcnt lgkmcnt(2)
	v_mfma_f32_16x16x32_bf16 v[0:3], v[8:11], v[16:19], v[0:3]
	ds_read_b128 v[8:11], v145 offset:896
	ds_read_b128 v[16:19], v145 offset:960
	s_waitcnt lgkmcnt(1)
	v_mfma_f32_16x16x32_bf16 v[0:3], v[4:7], v[8:11], v[0:3]
	ds_read_b128 v[4:7], v144 offset:34048
	s_waitcnt lgkmcnt(1)
	v_mfma_f32_16x16x32_bf16 v[0:3], v[12:15], v[16:19], v[0:3]
	ds_read_b128 v[8:11], v144 offset:34112
	ds_read_b128 v[12:15], v145 offset:1024
	ds_read_b128 v[16:19], v145 offset:1088
	s_waitcnt lgkmcnt(1)
	v_mfma_f32_16x16x32_bf16 v[0:3], v[4:7], v[12:15], v[0:3]
	ds_read_b128 v[4:7], v144 offset:34176
	ds_read_b128 v[12:15], v144 offset:34240
	s_waitcnt lgkmcnt(2)
	v_mfma_f32_16x16x32_bf16 v[0:3], v[8:11], v[16:19], v[0:3]
	ds_read_b128 v[8:11], v145 offset:1152
	ds_read_b128 v[16:19], v145 offset:1216
	s_waitcnt lgkmcnt(1)
	v_mfma_f32_16x16x32_bf16 v[0:3], v[4:7], v[8:11], v[0:3]
	ds_read_b128 v[4:7], v144 offset:34304
	ds_read_b128 v[8:11], v144 offset:34368
	s_waitcnt lgkmcnt(2)
	v_mfma_f32_16x16x32_bf16 v[0:3], v[12:15], v[16:19], v[0:3]
	ds_read_b128 v[12:15], v145 offset:1280
	ds_read_b128 v[16:19], v145 offset:1344
	s_waitcnt lgkmcnt(1)
	v_mfma_f32_16x16x32_bf16 v[0:3], v[4:7], v[12:15], v[0:3]
	ds_read_b128 v[4:7], v144 offset:34432
	ds_read_b128 v[12:15], v144 offset:34496
	s_waitcnt lgkmcnt(2)
	v_mfma_f32_16x16x32_bf16 v[0:3], v[8:11], v[16:19], v[0:3]
	ds_read_b128 v[8:11], v145 offset:1408
	ds_read_b128 v[16:19], v145 offset:1472
	s_waitcnt lgkmcnt(1)
	v_mfma_f32_16x16x32_bf16 v[0:3], v[4:7], v[8:11], v[0:3]
	ds_read_b128 v[4:7], v144 offset:34560
	s_waitcnt lgkmcnt(1)
	v_mfma_f32_16x16x32_bf16 v[0:3], v[12:15], v[16:19], v[0:3]
	ds_read_b128 v[8:11], v144 offset:34624
	ds_read_b128 v[12:15], v145 offset:1536
	ds_read_b128 v[16:19], v145 offset:1600
	s_waitcnt lgkmcnt(1)
	v_mfma_f32_16x16x32_bf16 v[0:3], v[4:7], v[12:15], v[0:3]
	ds_read_b128 v[4:7], v144 offset:34688
	ds_read_b128 v[12:15], v144 offset:34752
	s_waitcnt lgkmcnt(2)
	v_mfma_f32_16x16x32_bf16 v[0:3], v[8:11], v[16:19], v[0:3]
	ds_read_b128 v[8:11], v145 offset:1664
	ds_read_b128 v[16:19], v145 offset:1728
	s_waitcnt lgkmcnt(1)
	v_mfma_f32_16x16x32_bf16 v[0:3], v[4:7], v[8:11], v[0:3]
	ds_read_b128 v[4:7], v144 offset:34816
	ds_read_b128 v[8:11], v144 offset:34880
	s_waitcnt lgkmcnt(2)
	v_mfma_f32_16x16x32_bf16 v[0:3], v[12:15], v[16:19], v[0:3]
	ds_read_b128 v[12:15], v145 offset:1792
	ds_read_b128 v[16:19], v145 offset:1856
	s_waitcnt lgkmcnt(1)
	v_mfma_f32_16x16x32_bf16 v[0:3], v[4:7], v[12:15], v[0:3]
	ds_read_b128 v[4:7], v144 offset:34944
	ds_read_b128 v[12:15], v144 offset:35008
	s_waitcnt lgkmcnt(2)
	v_mfma_f32_16x16x32_bf16 v[0:3], v[8:11], v[16:19], v[0:3]
	ds_read_b128 v[8:11], v145 offset:1920
	ds_read_b128 v[16:19], v145 offset:1984
	s_waitcnt lgkmcnt(1)
	v_mfma_f32_16x16x32_bf16 v[0:3], v[4:7], v[8:11], v[0:3]
	s_waitcnt lgkmcnt(0)
	v_mfma_f32_16x16x32_bf16 v[0:3], v[12:15], v[16:19], v[0:3]
	s_and_saveexec_b64 s[30:31], s[4:5]
	s_cbranch_execz .LBB0_93
; DI float softplusf_(float x) { return fmaxf(x, 0.f) + log1pf(__expf(-fabsf(x))); }
; DI void phase_xnorm(const Params& p, int bid, int nb, char* lds) {
;     ...
;         else res = -__expf(p.a_log[j - 12]) * softplusf_(xx + p.dt_bias[j - 12]);
	s_and_saveexec_b64 s[34:35], s[6:7]
	s_xor_b64 s[34:35], exec, s[34:35]
	s_cbranch_execz .LBB0_101
	s_and_saveexec_b64 s[38:39], s[8:9]
	s_xor_b64 s[38:39], exec, s[38:39]
	s_cbranch_execz .LBB0_98
	v_mov_b32_e32 v4, v240
	v_mov_b32_e32 v5, v241
	v_add_f32_e32 v4, v0, v4
	v_mul_f32_e64 v6, |v4|, s18
	v_exp_f32_e32 v18, v6
	v_mul_f32_e32 v5, 0x3fb8aa3b, v5
	v_exp_f32_e32 v19, v5
	v_max_f32_e32 v20, 0, v4
	v_add_f32_e32 v6, 1.0, v18
	v_add_f32_e32 v7, -1.0, v6
	v_frexp_mant_f32_e32 v8, v6
	v_cvt_f64_f32_e32 v[4:5], v6
	v_sub_f32_e32 v9, v7, v6
	v_frexp_exp_i32_f64_e32 v4, v[4:5]
	v_cmp_gt_f32_e32 vcc, s19, v8
	v_sub_f32_e32 v7, v18, v7
	v_add_f32_e32 v5, 1.0, v9
	v_subbrev_co_u32_e32 v4, vcc, 0, v4, vcc
	v_add_f32_e32 v5, v7, v5
	v_sub_u32_e32 v7, 0, v4
	v_ldexp_f32 v6, v6, v7
	v_add_f32_e32 v8, -1.0, v6
	v_add_f32_e32 v9, 1.0, v6
	v_ldexp_f32 v5, v5, v7
	v_add_f32_e32 v7, 1.0, v8
	v_add_f32_e32 v10, -1.0, v9
	v_sub_f32_e32 v7, v6, v7
	v_sub_f32_e32 v6, v6, v10
	v_add_f32_e32 v10, v5, v7
	v_add_f32_e32 v5, v5, v6
	v_add_f32_e32 v12, v9, v5
	v_rcp_f32_e32 v13, v12
	v_add_f32_e32 v7, v8, v10
	v_sub_f32_e32 v8, v7, v8
	v_sub_f32_e32 v6, v12, v9
	v_mul_f32_e32 v15, v7, v13
	v_sub_f32_e32 v14, v10, v8
	v_mul_f32_e32 v8, v12, v15
	v_sub_f32_e32 v5, v5, v6
	v_fma_f32 v10, v15, v12, -v8
	v_fmac_f32_e32 v10, v15, v5
	v_add_f32_e32 v6, v8, v10
	v_sub_f32_e32 v9, v7, v6
	v_mov_b32_e32 v11, v6
	v_pk_add_f32 v[6:7], v[6:7], v[8:9] neg_lo:[0,1] neg_hi:[0,1]
	v_cvt_f32_i32_e32 v4, v4
	v_pk_add_f32 v[6:7], v[6:7], v[10:11] neg_lo:[0,1] neg_hi:[0,1]
	v_cmp_neq_f32_e32 vcc, s29, v18
	v_add_f32_e32 v7, v14, v7
	v_add_f32_e32 v6, v6, v7
	v_add_f32_e32 v7, v9, v6
	v_mul_f32_e32 v11, v13, v7
	v_mul_f32_e32 v8, v12, v11
	v_sub_f32_e32 v9, v9, v7
	v_add_f32_e32 v16, v15, v11
	v_fma_f32 v10, v11, v12, -v8
	v_add_f32_e32 v14, v6, v9
	v_sub_f32_e32 v6, v16, v15
	v_fmac_f32_e32 v10, v11, v5
	v_sub_f32_e32 v5, v11, v6
	v_add_f32_e32 v6, v8, v10
	v_sub_f32_e32 v9, v7, v6
	v_mov_b32_e32 v11, v6
	v_pk_add_f32 v[6:7], v[6:7], v[8:9] neg_lo:[0,1] neg_hi:[0,1]
	s_nop 0
	v_pk_add_f32 v[6:7], v[6:7], v[10:11] neg_lo:[0,1] neg_hi:[0,1]
	s_nop 0
	v_add_f32_e32 v7, v14, v7
	v_add_f32_e32 v6, v6, v7
	v_add_f32_e32 v6, v9, v6
	v_mul_f32_e32 v6, v13, v6
	v_add_f32_e32 v5, v5, v6
	v_add_f32_e32 v6, v16, v5
	v_mul_f32_e32 v8, v6, v6
	v_sub_f32_e32 v9, v6, v16
	v_fmamk_f32 v10, v8, 0x3e9b6dac, v148
	v_sub_f32_e32 v9, v5, v9
	v_mul_f32_e32 v5, v6, v8
	v_fmaak_f32 v115, v8, v10, 0x3f2aaada
	v_ldexp_f32 v11, v9, 1
	v_pk_mul_f32 v[8:9], v[4:5], v[114:115]
	v_ldexp_f32 v7, v6, 1
	v_fma_f32 v6, v4, s27, -v8
	v_fmac_f32_e32 v6, 0xb102e308, v4
	v_pk_add_f32 v[4:5], v[8:9], v[6:7]
	v_mov_b32_e32 v10, v8
	v_sub_f32_e32 v14, v5, v7
	v_pk_add_f32 v[12:13], v[4:5], v[8:9] neg_lo:[0,1] neg_hi:[0,1]
	v_sub_f32_e32 v8, v9, v14
	v_add_f32_e32 v11, v11, v8
	v_pk_add_f32 v[8:9], v[4:5], v[10:11]
	v_mov_b32_e32 v7, v4
	v_mov_b32_e32 v13, v9
	v_pk_add_f32 v[16:17], v[6:7], v[12:13] neg_lo:[0,1] neg_hi:[0,1]
	v_pk_add_f32 v[6:7], v[6:7], v[12:13]
	v_mov_b32_e32 v15, v4
	v_pk_add_f32 v[12:13], v[6:7], v[4:5] op_sel:[1,0] op_sel_hi:[0,1] neg_lo:[0,1] neg_hi:[0,1]
	v_mov_b32_e32 v14, v11
	v_mov_b32_e32 v10, v9
	v_mov_b32_e32 v11, v7
	v_pk_mov_b32 v[4:5], v[4:5], v[12:13] op_sel:[1,0]
	v_pk_add_f32 v[8:9], v[8:9], v[12:13] op_sel_hi:[1,0] neg_lo:[0,1] neg_hi:[0,1]
	v_pk_add_f32 v[4:5], v[10:11], v[4:5] neg_lo:[0,1] neg_hi:[0,1]
	v_mov_b32_e32 v8, v16
	v_pk_add_f32 v[4:5], v[14:15], v[4:5] neg_lo:[0,1] neg_hi:[0,1]
	v_mov_b32_e32 v17, v7
	v_pk_add_f32 v[8:9], v[8:9], v[4:5]
	s_nop 0
	v_pk_add_f32 v[10:11], v[8:9], v[8:9] op_sel:[0,1] op_sel_hi:[1,0]
	s_nop 0
	v_pk_add_f32 v[6:7], v[6:7], v[10:11] op_sel:[1,0] op_sel_hi:[0,1]
	v_mov_b32_e32 v9, v6
	v_mov_b32_e32 v5, v10
	v_pk_add_f32 v[10:11], v[8:9], v[16:17] neg_lo:[0,1] neg_hi:[0,1]
	s_nop 0
	v_sub_f32_e32 v7, v8, v10
	v_pk_add_f32 v[4:5], v[4:5], v[10:11] neg_lo:[0,1] neg_hi:[0,1]
	v_sub_f32_e32 v7, v16, v7
	v_add_f32_e32 v4, v4, v7
	v_add_f32_e32 v4, v4, v5
	v_add_f32_e32 v4, v6, v4
	v_cndmask_b32_e32 v4, v149, v4, vcc
	v_cmp_ngt_f32_e32 vcc, -1.0, v18
	s_nop 1
	v_cndmask_b32_e32 v4, v150, v4, vcc
	v_cmp_neq_f32_e32 vcc, -1.0, v18
	s_nop 1
	v_cndmask_b32_e32 v4, v151, v4, vcc
	v_cmp_lt_f32_e64 vcc, |v18|, s40
	s_nop 1
	v_cndmask_b32_e32 v4, v4, v18, vcc
	v_add_f32_e32 v4, v20, v4
	v_mul_f32_e64 v6, v4, -v19
